# v64 + the filler's store step moved behind the QK block (transposer reads in front of the moved K/V staging, counted wait + store behind it): nothing but the tile index in front of QK
# baseline (speedup 1.0000x reference)
; DEV int ltid() { int t = threadIdx.x; asm volatile("" : "+v"(t)); return t; }
; DEV void fill_store(CParams& p, int wg, int slot, int bufsel) {
;   extern __shared__ __attribute__((aligned(16))) char shm[];
;   const unsigned* T = (const unsigned*)(shm + FILL_LDS_OFF + bufsel * FILL_TB); const int tid = ltid(), nl = tid >> 3, cc = tid & 7;
;   const FillDesc d = fill_decode(p, wg, slot);
;   u32x4 v; v.x = T[nl * 33 + 4 * cc]; v.y = T[nl * 33 + 4 * cc + 1]; v.z = T[nl * 33 + 4 * cc + 2]; v.w = T[nl * 33 + 4 * cc + 3];
;   *(u32x4*)(d.dst + (long)perm_row(d.perm, d.n0 + nl) * 2048 + d.kh + 16 * cc) = v;
; }
; DEV void qkt(f32x16& p0, f32x16& p1, const char* Ks, const bf16x8* qr, int r32, int hi) {
;   p0 = f32x16{}; p1 = f32x16{};
;   __builtin_amdgcn_s_setprio(1);
; #pragma unroll
;   for (int d0 = 0; d0 < 12; ++d0) { const int cb = (d0 * 16 + hi * 8) * 2;
;     const bf16x8 b0 = *reinterpret_cast<const bf16x8*>(Ks + KSWZ2(r32, cb));
;     const bf16x8 b1 = *reinterpret_cast<const bf16x8*>(Ks + KSWZ2(32 + r32, cb));
;     p0 = __builtin_amdgcn_mfma_f32_32x32x16_bf16(b0, qr[d0], p0, 0, 0, 0);
;     p1 = __builtin_amdgcn_mfma_f32_32x32x16_bf16(b1, qr[d0], p1, 0, 0, 0); }
;   __builtin_amdgcn_s_setprio(0);
; }
.LBB0_899:
.LBB0_907:
	s_lshl_b32 s6, s36, 15
	s_add_i32 s6, s6, 0
	s_setprio 1
	v_add3_u32 v66, s6, v201, v200
	ds_read_b128 v[68:71], v66 offset:32768
	ds_read_b128 v[72:75], v66 offset:49152
	v_add3_u32 v66, s6, v202, v200
	ds_read_b128 v[224:227], v66 offset:32768
	ds_read_b128 v[228:231], v66 offset:49152
	v_add3_u32 v66, s6, v203, v200
	s_waitcnt lgkmcnt(0)
	v_mfma_f32_32x32x16_bf16 v[84:99], v[68:71], v[100:103], 0
	v_mfma_f32_32x32x16_bf16 v[68:83], v[72:75], v[100:103], 0
	v_mfma_f32_32x32x16_bf16 v[84:99], v[224:227], v[104:107], v[84:99]
	v_mfma_f32_32x32x16_bf16 v[68:83], v[228:231], v[104:107], v[68:83]
	ds_read_b128 v[224:227], v66 offset:32768
	ds_read_b128 v[228:231], v66 offset:49152
	v_add3_u32 v66, s6, v204, v200
	s_waitcnt lgkmcnt(1)
	v_mfma_f32_32x32x16_bf16 v[84:99], v[224:227], v[108:111], v[84:99]
	s_waitcnt lgkmcnt(0)
	v_mfma_f32_32x32x16_bf16 v[68:83], v[228:231], v[108:111], v[68:83]
	ds_read_b128 v[224:227], v66 offset:32768
	ds_read_b128 v[228:231], v66 offset:49152
	v_add3_u32 v66, s6, v205, v200
	s_waitcnt lgkmcnt(1)
	v_mfma_f32_32x32x16_bf16 v[84:99], v[224:227], v[112:115], v[84:99]
	s_waitcnt lgkmcnt(0)
	v_mfma_f32_32x32x16_bf16 v[68:83], v[228:231], v[112:115], v[68:83]
	ds_read_b128 v[224:227], v66 offset:32768
	ds_read_b128 v[228:231], v66 offset:49152
	v_add3_u32 v66, s6, v206, v200
	s_waitcnt lgkmcnt(1)
	v_mfma_f32_32x32x16_bf16 v[84:99], v[224:227], v[116:119], v[84:99]
	s_waitcnt lgkmcnt(0)
	v_mfma_f32_32x32x16_bf16 v[68:83], v[228:231], v[116:119], v[68:83]
	ds_read_b128 v[224:227], v66 offset:32768
	ds_read_b128 v[228:231], v66 offset:49152
	v_add3_u32 v66, s6, v207, v200
	s_waitcnt lgkmcnt(1)
	v_mfma_f32_32x32x16_bf16 v[84:99], v[224:227], v[120:123], v[84:99]
	s_waitcnt lgkmcnt(0)
	v_mfma_f32_32x32x16_bf16 v[68:83], v[228:231], v[120:123], v[68:83]
	ds_read_b128 v[224:227], v66 offset:32768
	ds_read_b128 v[228:231], v66 offset:49152
	v_add3_u32 v66, s6, v208, v200
	s_waitcnt lgkmcnt(1)
	v_mfma_f32_32x32x16_bf16 v[84:99], v[224:227], v[124:127], v[84:99]
	s_waitcnt lgkmcnt(0)
	v_mfma_f32_32x32x16_bf16 v[68:83], v[228:231], v[124:127], v[68:83]
	ds_read_b128 v[224:227], v66 offset:32768
	ds_read_b128 v[228:231], v66 offset:49152
	v_add3_u32 v66, s6, v209, v200
	s_waitcnt lgkmcnt(1)
	v_mfma_f32_32x32x16_bf16 v[84:99], v[224:227], v[128:131], v[84:99]
	s_waitcnt lgkmcnt(0)
	v_mfma_f32_32x32x16_bf16 v[68:83], v[228:231], v[128:131], v[68:83]
	ds_read_b128 v[224:227], v66 offset:32768
	ds_read_b128 v[228:231], v66 offset:49152
	v_add3_u32 v66, s6, v211, v200
	s_waitcnt lgkmcnt(1)
	v_mfma_f32_32x32x16_bf16 v[84:99], v[224:227], v[132:135], v[84:99]
	s_waitcnt lgkmcnt(0)
	v_mfma_f32_32x32x16_bf16 v[68:83], v[228:231], v[132:135], v[68:83]
	ds_read_b128 v[224:227], v66 offset:32768
	ds_read_b128 v[228:231], v66 offset:49152
	v_add3_u32 v66, s6, v212, v200
	s_waitcnt lgkmcnt(1)
	v_mfma_f32_32x32x16_bf16 v[84:99], v[224:227], v[140:143], v[84:99]
	s_waitcnt lgkmcnt(0)
	v_mfma_f32_32x32x16_bf16 v[68:83], v[228:231], v[140:143], v[68:83]
	ds_read_b128 v[224:227], v66 offset:32768
	ds_read_b128 v[228:231], v66 offset:49152
	v_add3_u32 v66, s6, v213, v200
	s_waitcnt lgkmcnt(1)
	v_mfma_f32_32x32x16_bf16 v[84:99], v[224:227], v[136:139], v[84:99]
	s_waitcnt lgkmcnt(0)
	v_mfma_f32_32x32x16_bf16 v[68:83], v[228:231], v[136:139], v[68:83]
	ds_read_b128 v[224:227], v66 offset:32768
	ds_read_b128 v[228:231], v66 offset:49152
	s_waitcnt lgkmcnt(1)
	v_mfma_f32_32x32x16_bf16 v[84:99], v[224:227], v[144:147], v[84:99]
	s_waitcnt lgkmcnt(0)
	v_mfma_f32_32x32x16_bf16 v[68:83], v[228:231], v[144:147], v[68:83]
	s_setprio 0
	s_cmp_gt_u32 s35, 62
	s_cbranch_scc1 .Lt3r_a
	s_xor_b32 s56, s36, 1
	s_mul_i32 s56, s56, 0x2200
	v_add_u32_e32 v253, s56, v244
	ds_read2_b32 v[224:225], v253 offset1:1
	ds_read2_b32 v[226:227], v253 offset0:2 offset1:3
.Lt3r_a:
	s_cmpk_eq_i32 s34, 0x41
	s_cbranch_scc1 .Lmv1_a
	s_cmp_gt_u32 s34, 60
	s_mov_b64 s[6:7], -1
	s_cbranch_scc0 .LBB0_895
	s_waitcnt vmcnt(0)
	s_mov_b64 s[6:7], 0

; DEV int ltid() { int t = threadIdx.x; asm volatile("" : "+v"(t)); return t; }
; DEV void fill_store(CParams& p, int wg, int slot, int bufsel) {
;   extern __shared__ __attribute__((aligned(16))) char shm[];
;   const unsigned* T = (const unsigned*)(shm + FILL_LDS_OFF + bufsel * FILL_TB); const int tid = ltid(), nl = tid >> 3, cc = tid & 7;
;   const FillDesc d = fill_decode(p, wg, slot);
;   u32x4 v; v.x = T[nl * 33 + 4 * cc]; v.y = T[nl * 33 + 4 * cc + 1]; v.z = T[nl * 33 + 4 * cc + 2]; v.w = T[nl * 33 + 4 * cc + 3];
;   *(u32x4*)(d.dst + (long)perm_row(d.perm, d.n0 + nl) * 2048 + d.kh + 16 * cc) = v;
; }
.Lmv2_a:
	s_cmp_gt_u32 s35, 62
	s_cbranch_scc1 .Lt3s_a
	s_add_i32 s57, s37, 66
	s_cmp_gt_u32 s57, 0x7f
	s_cbranch_scc1 .Lt3d_a
	s_lshr_b32 s58, s57, 2
	s_lshl_b32 s58, s58, 23
	s_and_b32 s59, s57, 3
	s_lshl_b32 s59, s59, 9
	s_or_b32 s58, s58, s59
	s_add_u32 s60, s12, s58
	s_addc_u32 s61, s13, 0
	s_waitcnt lgkmcnt(5)
	global_store_dwordx4 v246, v[224:227], s[60:61]
	s_branch .Lt3s_a
.Lt3d_a:
	s_sub_u32 s57, s57, 0x80
	s_lshr_b32 s58, s57, 1
	s_lshl_b32 s58, s58, 22
	s_and_b32 s59, s57, 1
	s_lshl_b32 s59, s59, 10
	s_or_b32 s58, s58, s59
	s_add_u32 s60, s14, s58
	s_addc_u32 s61, s15, 0
	s_waitcnt lgkmcnt(5)
	global_store_dwordx4 v247, v[224:227], s[60:61]

; DEV int ltid() { int t = threadIdx.x; asm volatile("" : "+v"(t)); return t; }
; DEV void fill_store(CParams& p, int wg, int slot, int bufsel) {
;   extern __shared__ __attribute__((aligned(16))) char shm[];
;   const unsigned* T = (const unsigned*)(shm + FILL_LDS_OFF + bufsel * FILL_TB); const int tid = ltid(), nl = tid >> 3, cc = tid & 7;
;   const FillDesc d = fill_decode(p, wg, slot);
;   u32x4 v; v.x = T[nl * 33 + 4 * cc]; v.y = T[nl * 33 + 4 * cc + 1]; v.z = T[nl * 33 + 4 * cc + 2]; v.w = T[nl * 33 + 4 * cc + 3];
;   *(u32x4*)(d.dst + (long)perm_row(d.perm, d.n0 + nl) * 2048 + d.kh + 16 * cc) = v;
; }
; DEV void qkt(f32x16& p0, f32x16& p1, const char* Ks, const bf16x8* qr, int r32, int hi) {
;   p0 = f32x16{}; p1 = f32x16{};
;   __builtin_amdgcn_s_setprio(1);
; #pragma unroll
;   for (int d0 = 0; d0 < 12; ++d0) { const int cb = (d0 * 16 + hi * 8) * 2;
;     const bf16x8 b0 = *reinterpret_cast<const bf16x8*>(Ks + KSWZ2(r32, cb));
;     const bf16x8 b1 = *reinterpret_cast<const bf16x8*>(Ks + KSWZ2(32 + r32, cb));
;     p0 = __builtin_amdgcn_mfma_f32_32x32x16_bf16(b0, qr[d0], p0, 0, 0, 0);
;     p1 = __builtin_amdgcn_mfma_f32_32x32x16_bf16(b1, qr[d0], p1, 0, 0, 0); }
;   __builtin_amdgcn_s_setprio(0);
; }
.LBB0_1106:
.LBB0_1114:
	s_lshl_b32 s6, s37, 15
	s_add_i32 s6, s6, 0
	s_setprio 1
	v_add3_u32 v66, s6, v201, v200
	ds_read_b128 v[68:71], v66 offset:32768
	ds_read_b128 v[72:75], v66 offset:49152
	v_add3_u32 v66, s6, v202, v200
	ds_read_b128 v[224:227], v66 offset:32768
	ds_read_b128 v[228:231], v66 offset:49152
	v_add3_u32 v66, s6, v203, v200
	s_waitcnt lgkmcnt(0)
	v_mfma_f32_32x32x16_bf16 v[84:99], v[68:71], v[100:103], 0
	v_mfma_f32_32x32x16_bf16 v[68:83], v[72:75], v[100:103], 0
	v_mfma_f32_32x32x16_bf16 v[84:99], v[224:227], v[104:107], v[84:99]
	v_mfma_f32_32x32x16_bf16 v[68:83], v[228:231], v[104:107], v[68:83]
	ds_read_b128 v[224:227], v66 offset:32768
	ds_read_b128 v[228:231], v66 offset:49152
	v_add3_u32 v66, s6, v204, v200
	s_waitcnt lgkmcnt(1)
	v_mfma_f32_32x32x16_bf16 v[84:99], v[224:227], v[108:111], v[84:99]
	s_waitcnt lgkmcnt(0)
	v_mfma_f32_32x32x16_bf16 v[68:83], v[228:231], v[108:111], v[68:83]
	ds_read_b128 v[224:227], v66 offset:32768
	ds_read_b128 v[228:231], v66 offset:49152
	v_add3_u32 v66, s6, v205, v200
	s_waitcnt lgkmcnt(1)
	v_mfma_f32_32x32x16_bf16 v[84:99], v[224:227], v[112:115], v[84:99]
	s_waitcnt lgkmcnt(0)
	v_mfma_f32_32x32x16_bf16 v[68:83], v[228:231], v[112:115], v[68:83]
	ds_read_b128 v[224:227], v66 offset:32768
	ds_read_b128 v[228:231], v66 offset:49152
	v_add3_u32 v66, s6, v206, v200
	s_waitcnt lgkmcnt(1)
	v_mfma_f32_32x32x16_bf16 v[84:99], v[224:227], v[116:119], v[84:99]
	s_waitcnt lgkmcnt(0)
	v_mfma_f32_32x32x16_bf16 v[68:83], v[228:231], v[116:119], v[68:83]
	ds_read_b128 v[224:227], v66 offset:32768
	ds_read_b128 v[228:231], v66 offset:49152
	v_add3_u32 v66, s6, v207, v200
	s_waitcnt lgkmcnt(1)
	v_mfma_f32_32x32x16_bf16 v[84:99], v[224:227], v[120:123], v[84:99]
	s_waitcnt lgkmcnt(0)
	v_mfma_f32_32x32x16_bf16 v[68:83], v[228:231], v[120:123], v[68:83]
	ds_read_b128 v[224:227], v66 offset:32768
	ds_read_b128 v[228:231], v66 offset:49152
	v_add3_u32 v66, s6, v208, v200
	s_waitcnt lgkmcnt(1)
	v_mfma_f32_32x32x16_bf16 v[84:99], v[224:227], v[124:127], v[84:99]
	s_waitcnt lgkmcnt(0)
	v_mfma_f32_32x32x16_bf16 v[68:83], v[228:231], v[124:127], v[68:83]
	ds_read_b128 v[224:227], v66 offset:32768
	ds_read_b128 v[228:231], v66 offset:49152
	v_add3_u32 v66, s6, v209, v200
	s_waitcnt lgkmcnt(1)
	v_mfma_f32_32x32x16_bf16 v[84:99], v[224:227], v[128:131], v[84:99]
	s_waitcnt lgkmcnt(0)
	v_mfma_f32_32x32x16_bf16 v[68:83], v[228:231], v[128:131], v[68:83]
	ds_read_b128 v[224:227], v66 offset:32768
	ds_read_b128 v[228:231], v66 offset:49152
	v_add3_u32 v66, s6, v211, v200
	s_waitcnt lgkmcnt(1)
	v_mfma_f32_32x32x16_bf16 v[84:99], v[224:227], v[132:135], v[84:99]
	s_waitcnt lgkmcnt(0)
	v_mfma_f32_32x32x16_bf16 v[68:83], v[228:231], v[132:135], v[68:83]
	ds_read_b128 v[224:227], v66 offset:32768
	ds_read_b128 v[228:231], v66 offset:49152
	v_add3_u32 v66, s6, v212, v200
	s_waitcnt lgkmcnt(1)
	v_mfma_f32_32x32x16_bf16 v[84:99], v[224:227], v[140:143], v[84:99]
	s_waitcnt lgkmcnt(0)
	v_mfma_f32_32x32x16_bf16 v[68:83], v[228:231], v[140:143], v[68:83]
	ds_read_b128 v[224:227], v66 offset:32768
	ds_read_b128 v[228:231], v66 offset:49152
	v_add3_u32 v66, s6, v213, v200
	s_waitcnt lgkmcnt(1)
	v_mfma_f32_32x32x16_bf16 v[84:99], v[224:227], v[136:139], v[84:99]
	s_waitcnt lgkmcnt(0)
	v_mfma_f32_32x32x16_bf16 v[68:83], v[228:231], v[136:139], v[68:83]
	ds_read_b128 v[224:227], v66 offset:32768
	ds_read_b128 v[228:231], v66 offset:49152
	s_waitcnt lgkmcnt(1)
	v_mfma_f32_32x32x16_bf16 v[84:99], v[224:227], v[144:147], v[84:99]
	s_waitcnt lgkmcnt(0)
	v_mfma_f32_32x32x16_bf16 v[68:83], v[228:231], v[144:147], v[68:83]
	s_setprio 0
	s_cmp_gt_u32 s36, 61
	s_cbranch_scc1 .Lt3r_b
	s_xor_b32 s56, s37, 1
	s_mul_i32 s56, s56, 0x2200
	v_add_u32_e32 v253, s56, v244
	ds_read2_b32 v[224:225], v253 offset1:1
	ds_read2_b32 v[226:227], v253 offset0:2 offset1:3
.Lt3r_b:
	s_cmpk_eq_i32 s35, 0x41
	s_cbranch_scc1 .Lmv1_b
	s_cmp_gt_u32 s35, 59
	s_mov_b64 s[6:7], -1
	s_cbranch_scc0 .LBB0_1102
	s_waitcnt vmcnt(0)
	s_mov_b64 s[6:7], 0

; DEV int ltid() { int t = threadIdx.x; asm volatile("" : "+v"(t)); return t; }
; DEV void fill_store(CParams& p, int wg, int slot, int bufsel) {
;   extern __shared__ __attribute__((aligned(16))) char shm[];
;   const unsigned* T = (const unsigned*)(shm + FILL_LDS_OFF + bufsel * FILL_TB); const int tid = ltid(), nl = tid >> 3, cc = tid & 7;
;   const FillDesc d = fill_decode(p, wg, slot);
;   u32x4 v; v.x = T[nl * 33 + 4 * cc]; v.y = T[nl * 33 + 4 * cc + 1]; v.z = T[nl * 33 + 4 * cc + 2]; v.w = T[nl * 33 + 4 * cc + 3];
;   *(u32x4*)(d.dst + (long)perm_row(d.perm, d.n0 + nl) * 2048 + d.kh + 16 * cc) = v;
; }
.Lmv2_b:
	s_cmp_gt_u32 s36, 61
	s_cbranch_scc1 .Lt3s_b
	s_add_i32 s57, s38, 129
	s_sub_u32 s57, s57, 0x80
	s_lshr_b32 s58, s57, 1
	s_lshl_b32 s58, s58, 22
	s_and_b32 s59, s57, 1
	s_lshl_b32 s59, s59, 10
	s_or_b32 s58, s58, s59
	s_add_u32 s60, s14, s58
	s_addc_u32 s61, s15, 0
	s_waitcnt lgkmcnt(5)
	global_store_dwordx4 v247, v[224:227], s[60:61]
